# P7 router top-4: lane-parallel DPP max + ballot/ff1 per round instead of the 4x32 scalar compare chain in 4 redundant lanes
# speedup vs baseline: 1.0222x; 1.0080x over previous
; #define LAS __attribute__((address_space(3)))
; template <bool FAST>
; __device__ __forceinline__ void p7_route_t(Frame& F, const bool do_route) {
;     ...
;         float lg[NE];
; #pragma unroll
;         for (int e4 = 0; e4 < NE / 4; ++e4) { const f32x4 t = *(const LAS f32x4*)(lgb + F.wave * 32 + 4 * e4); lg[4 * e4] = t.x; lg[4 * e4 + 1] = t.y; lg[4 * e4 + 2] = t.z; lg[4 * e4 + 3] = t.w; }
;         unsigned taken = 0u; int es[TOPK]; float vs[TOPK];
; #pragma unroll
;         for (int k = 0; k < TOPK; ++k) { float best = -3.0e38f; int bi = 0;
; #pragma unroll
;             for (int e = 0; e < NE; ++e) { const bool ok = !((taken >> e) & 1u) && lg[e] > best; best = ok ? lg[e] : best; bi = ok ? e : bi; }
;             taken |= 1u << bi; es[k] = bi; vs[k] = best; }
;         float ps[TOPK], psum = 0.f;
; #pragma unroll
;         for (int k = 0; k < TOPK; ++k) { ps[k] = __expf(vs[k] - vs[0]); psum += ps[k]; }
;         if (do_route && valid && F.lane < TOPK) {
;             const int k = F.lane; const int e = k == 0 ? es[0] : k == 1 ? es[1] : k == 2 ? es[2] : es[3]; const float p = k == 0 ? ps[0] : k == 1 ? ps[1] : k == 2 ? ps[2] : ps[3];
;             const int lr = (int)__hip_atomic_fetch_add(lcnt + e, 1u, __ATOMIC_RELAXED, __HIP_MEMORY_SCOPE_WORKGROUP);
;             tok_e[row * TOPK + k] = e; tok_rank[row * TOPK + k] = lr; tok_gate[row * TOPK + k] = p / psum;
;         }
.LBB0_832:
	s_or_b64 exec, exec, s[2:3]
	s_nor_b64 s[0:1], s[0:1], s[4:5]
	s_waitcnt lgkmcnt(0)
	s_barrier
	s_and_saveexec_b64 s[28:29], s[0:1]
	s_cbranch_execz .LBB0_789
	v_readlane_b32 s0, v254, 42
	s_nop 1
	s_mov_b64 s[98:99], exec
	s_mov_b32 exec_lo, -1
	s_mov_b32 exec_hi, 0
	v_lshl_add_u32 v2, v1, 2, s0
	ds_read_b32 v2, v2
	v_mov_b32_e32 v8, 0xff800000
	s_waitcnt lgkmcnt(0)
	v_max_f32_e32 v2, 0xff61b1e6, v2
	s_nop 1
	v_max_f32_dpp v3, v2, v2 quad_perm:[1,0,3,2] row_mask:0xf bank_mask:0xf
	s_nop 1
	v_max_f32_dpp v3, v3, v3 quad_perm:[2,3,0,1] row_mask:0xf bank_mask:0xf
	s_nop 1
	v_max_f32_dpp v3, v3, v3 row_ror:4 row_mask:0xf bank_mask:0xf
	s_nop 1
	v_max_f32_dpp v3, v3, v3 row_ror:8 row_mask:0xf bank_mask:0xf
	s_nop 1
	v_readlane_b32 s2, v3, 0
	v_readlane_b32 s3, v3, 16
	s_nop 1
	v_mov_b32_e32 v4, s3
	v_max_f32_e32 v4, s2, v4
	v_cmp_eq_f32_e32 vcc, v2, v4
	v_mov_b32_e32 v45, v4
	s_nop 3
	s_ff1_i32_b32 s16, vcc_lo
	s_max_i32 s16, s16, 0
	v_cmp_eq_u32_e32 vcc, s16, v1
	s_nop 1
	v_cndmask_b32_e32 v2, v2, v8, vcc
	s_nop 1
	v_max_f32_dpp v3, v2, v2 quad_perm:[1,0,3,2] row_mask:0xf bank_mask:0xf
	s_nop 1
	v_max_f32_dpp v3, v3, v3 quad_perm:[2,3,0,1] row_mask:0xf bank_mask:0xf
	s_nop 1
	v_max_f32_dpp v3, v3, v3 row_ror:4 row_mask:0xf bank_mask:0xf
	s_nop 1
	v_max_f32_dpp v3, v3, v3 row_ror:8 row_mask:0xf bank_mask:0xf
	s_nop 1
	v_readlane_b32 s2, v3, 0
	v_readlane_b32 s3, v3, 16
	s_nop 1
	v_mov_b32_e32 v4, s3
	v_max_f32_e32 v4, s2, v4
	v_cmp_eq_f32_e32 vcc, v2, v4
	v_mov_b32_e32 v46, v4
	s_nop 3
	s_ff1_i32_b32 s17, vcc_lo
	s_max_i32 s17, s17, 0
	v_cmp_eq_u32_e32 vcc, s17, v1
	s_nop 1
	v_cndmask_b32_e32 v2, v2, v8, vcc
	s_nop 1
	v_max_f32_dpp v3, v2, v2 quad_perm:[1,0,3,2] row_mask:0xf bank_mask:0xf
	s_nop 1
	v_max_f32_dpp v3, v3, v3 quad_perm:[2,3,0,1] row_mask:0xf bank_mask:0xf
	s_nop 1
	v_max_f32_dpp v3, v3, v3 row_ror:4 row_mask:0xf bank_mask:0xf
	s_nop 1
	v_max_f32_dpp v3, v3, v3 row_ror:8 row_mask:0xf bank_mask:0xf
	s_nop 1
	v_readlane_b32 s2, v3, 0
	v_readlane_b32 s3, v3, 16
	s_nop 1
	v_mov_b32_e32 v4, s3
	v_max_f32_e32 v4, s2, v4
	v_cmp_eq_f32_e32 vcc, v2, v4
	v_mov_b32_e32 v47, v4
	s_nop 3
	s_ff1_i32_b32 s18, vcc_lo
	s_max_i32 s18, s18, 0
	v_cmp_eq_u32_e32 vcc, s18, v1
	s_nop 1
	v_cndmask_b32_e32 v2, v2, v8, vcc
	s_nop 1
	v_max_f32_dpp v3, v2, v2 quad_perm:[1,0,3,2] row_mask:0xf bank_mask:0xf
	s_nop 1
	v_max_f32_dpp v3, v3, v3 quad_perm:[2,3,0,1] row_mask:0xf bank_mask:0xf
	s_nop 1
	v_max_f32_dpp v3, v3, v3 row_ror:4 row_mask:0xf bank_mask:0xf
	s_nop 1
	v_max_f32_dpp v3, v3, v3 row_ror:8 row_mask:0xf bank_mask:0xf
	s_nop 1
	v_readlane_b32 s2, v3, 0
	v_readlane_b32 s3, v3, 16
	s_nop 1
	v_mov_b32_e32 v4, s3
	v_max_f32_e32 v4, s2, v4
	v_cmp_eq_f32_e32 vcc, v2, v4
	v_mov_b32_e32 v5, v4
	s_nop 3
	s_ff1_i32_b32 s19, vcc_lo
	s_max_i32 s19, s19, 0
	s_mov_b64 exec, s[98:99]
	v_sub_f32_e32 v44, v45, v45
	v_sub_f32_e32 v46, v46, v45
	v_sub_f32_e32 v47, v47, v45
	v_sub_f32_e32 v2, v5, v45
	v_mul_f32_e32 v44, 0x3fb8aa3b, v44
	v_mul_f32_e32 v46, 0x3fb8aa3b, v46
	v_mul_f32_e32 v47, 0x3fb8aa3b, v47
	v_mul_f32_e32 v2, 0x3fb8aa3b, v2
	v_exp_f32_e32 v44, v44
	v_exp_f32_e32 v46, v46
	v_exp_f32_e32 v47, v47
	v_exp_f32_e32 v2, v2
	v_mov_b32_e32 v3, s19
	v_mov_b32_e32 v4, s18
	v_cndmask_b32_e64 v3, v3, v4, s[14:15]
	v_mov_b32_e32 v4, s17
	v_cndmask_b32_e64 v3, v3, v4, s[12:13]
	v_mov_b32_e32 v4, s16
	v_cndmask_b32_e64 v7, v3, v4, s[10:11]
	v_add_f32_e32 v3, 0, v44
	v_add_f32_e32 v3, v3, v46
	v_add_f32_e32 v3, v3, v47
	v_add_f32_e32 v6, v3, v2
	v_cndmask_b32_e64 v2, v2, v47, s[14:15]
	v_cndmask_b32_e64 v2, v2, v46, s[12:13]
	v_cndmask_b32_e64 v8, v2, v44, s[10:11]
	v_lshl_add_u32 v2, v7, 2, 0
	ds_add_rtn_u32 v9, v2, v109
	v_lshl_or_b32 v2, s90, 2, v1
	v_div_scale_f32 v10, s[0:1], v6, v6, v8
	v_ashrrev_i32_e32 v3, 31, v2
	v_rcp_f32_e32 v11, v10
	v_lshlrev_b64 v[2:3], 2, v[2:3]
	v_lshl_add_u64 v[4:5], s[82:83], 0, v[2:3]
	global_store_dword v[4:5], v7, off
	v_lshl_add_u64 v[4:5], s[86:87], 0, v[2:3]
	s_waitcnt lgkmcnt(0)
	global_store_dword v[4:5], v9, off
	v_fma_f32 v4, -v10, v11, 1.0
	v_fmac_f32_e32 v11, v4, v11
	v_div_scale_f32 v4, vcc, v8, v6, v8
	v_mul_f32_e32 v5, v4, v11
	v_fma_f32 v7, -v10, v5, v4
	v_fmac_f32_e32 v5, v7, v11
	v_fma_f32 v4, -v10, v5, v4
	v_readlane_b32 s0, v254, 33
	v_readlane_b32 s66, v254, 36
	v_div_fmas_f32 v4, v4, v11, v5
	v_readlane_b32 s1, v254, 34
	v_readlane_b32 s67, v254, 37
	v_readlane_b32 s79, v254, 38
	v_div_fixup_f32 v4, v4, v6, v8
	v_lshl_add_u64 v[2:3], s[0:1], 0, v[2:3]
	global_store_dword v[2:3], v4, off
	s_branch .LBB0_789
